# GEMM unit start: the 128 accumulator-zeroing v_mov_b32 replaced by 64 v_mov_b64 (in-proj, w_out, MoE1, MoE2)
# baseline (speedup 1.0000x reference)
.LBB0_261:
	s_ashr_i32 s21, s20, 31
	s_lshl_b64 s[58:59], s[20:21], 19
	s_add_u32 s58, s88, s58
	s_addc_u32 s59, s89, s59
	s_and_b64 s[62:63], s[26:27], exec
	s_cselect_b32 s21, s59, s77
	s_cselect_b32 s68, s58, s76
	s_ashr_i32 s19, s18, 31
	s_lshl_b64 s[62:63], s[18:19], 19
	s_add_u32 s62, s10, s62
	s_addc_u32 s63, s11, s63
	s_and_b64 s[72:73], s[26:27], exec
	s_cselect_b32 s19, s63, s79
	s_cselect_b32 s69, s62, s78
	s_add_u32 s76, s76, 0x40080
	s_addc_u32 s77, s77, 0
	s_add_u32 s71, s78, 0x100
	v_mov_b32_e32 v34, 0
	s_addc_u32 s72, s79, 0
	s_mov_b32 s73, -2
	v_mov_b64_e32 v[36:37], 0
	v_mov_b64_e32 v[38:39], 0
	v_mov_b64_e32 v[40:41], 0
	v_mov_b64_e32 v[42:43], 0
	v_mov_b64_e32 v[44:45], 0
	v_mov_b64_e32 v[46:47], 0
	v_mov_b64_e32 v[48:49], 0
	v_mov_b64_e32 v[50:51], 0
	v_mov_b64_e32 v[52:53], 0
	v_mov_b64_e32 v[54:55], 0
	v_mov_b64_e32 v[56:57], 0
	v_mov_b64_e32 v[58:59], 0
	v_mov_b64_e32 v[60:61], 0
	v_mov_b64_e32 v[62:63], 0
	v_mov_b64_e32 v[64:65], 0
	v_mov_b64_e32 v[66:67], 0
	v_mov_b64_e32 v[68:69], 0
	v_mov_b64_e32 v[70:71], 0
	v_mov_b64_e32 v[72:73], 0
	v_mov_b64_e32 v[74:75], 0
	v_mov_b64_e32 v[76:77], 0
	v_mov_b64_e32 v[78:79], 0
	v_mov_b64_e32 v[80:81], 0
	v_mov_b64_e32 v[82:83], 0
	v_mov_b64_e32 v[84:85], 0
	v_mov_b64_e32 v[86:87], 0
	v_mov_b64_e32 v[88:89], 0
	v_mov_b64_e32 v[90:91], 0
	v_mov_b64_e32 v[92:93], 0
	v_mov_b64_e32 v[94:95], 0
	v_mov_b64_e32 v[96:97], 0
	v_mov_b64_e32 v[98:99], 0
	v_mov_b64_e32 v[100:101], 0
	v_mov_b64_e32 v[102:103], 0
	v_mov_b64_e32 v[104:105], 0
	v_mov_b64_e32 v[106:107], 0
	v_mov_b64_e32 v[108:109], 0
	v_mov_b64_e32 v[110:111], 0
	v_mov_b64_e32 v[112:113], 0
	v_mov_b64_e32 v[114:115], 0
	v_mov_b64_e32 v[116:117], 0
	v_mov_b64_e32 v[118:119], 0
	v_mov_b64_e32 v[120:121], 0
	v_mov_b64_e32 v[122:123], 0
	v_mov_b64_e32 v[124:125], 0
	v_mov_b64_e32 v[126:127], 0
	v_mov_b64_e32 v[128:129], 0
	v_mov_b64_e32 v[130:131], 0
	v_mov_b64_e32 v[132:133], 0
	v_mov_b64_e32 v[134:135], 0
	v_mov_b64_e32 v[136:137], 0
	v_mov_b64_e32 v[138:139], 0
	v_mov_b64_e32 v[140:141], 0
	v_mov_b64_e32 v[142:143], 0
	v_mov_b64_e32 v[144:145], 0
	v_mov_b64_e32 v[146:147], 0
	v_mov_b64_e32 v[148:149], 0
	v_mov_b64_e32 v[150:151], 0
	v_mov_b64_e32 v[152:153], 0
	v_mov_b64_e32 v[154:155], 0
	v_mov_b64_e32 v[156:157], 0
	v_mov_b64_e32 v[158:159], 0
	v_mov_b64_e32 v[160:161], 0
	v_mov_b64_e32 v[34:35], 0

.LBB0_1344:
	s_ashr_i32 s27, s26, 31
	s_lshl_b64 s[54:55], s[26:27], 19
	s_add_u32 s54, s4, s54
	s_addc_u32 s55, s5, s55
	s_and_b64 s[56:57], s[52:53], exec
	s_cselect_b32 s27, s55, s63
	s_cselect_b32 s75, s54, s62
	s_ashr_i32 s25, s24, 31
	s_lshl_b64 s[56:57], s[24:25], 19
	s_add_u32 s56, s86, s56
	s_addc_u32 s57, s87, s57
	s_and_b64 s[72:73], s[52:53], exec
	s_cselect_b32 s25, s57, s71
	s_cselect_b32 s76, s56, s70
	s_add_u32 s62, s62, 0x40080
	s_addc_u32 s63, s63, 0
	s_add_u32 s77, s70, 0x100
	v_mov_b32_e32 v34, 0
	s_addc_u32 s78, s71, 0
	s_mov_b32 s79, -2
	v_mov_b64_e32 v[36:37], 0
	v_mov_b64_e32 v[38:39], 0
	v_mov_b64_e32 v[40:41], 0
	v_mov_b64_e32 v[42:43], 0
	v_mov_b64_e32 v[44:45], 0
	v_mov_b64_e32 v[46:47], 0
	v_mov_b64_e32 v[48:49], 0
	v_mov_b64_e32 v[50:51], 0
	v_mov_b64_e32 v[52:53], 0
	v_mov_b64_e32 v[54:55], 0
	v_mov_b64_e32 v[56:57], 0
	v_mov_b64_e32 v[58:59], 0
	v_mov_b64_e32 v[60:61], 0
	v_mov_b64_e32 v[62:63], 0
	v_mov_b64_e32 v[64:65], 0
	v_mov_b64_e32 v[66:67], 0
	v_mov_b64_e32 v[68:69], 0
	v_mov_b64_e32 v[70:71], 0
	v_mov_b64_e32 v[72:73], 0
	v_mov_b64_e32 v[74:75], 0
	v_mov_b64_e32 v[76:77], 0
	v_mov_b64_e32 v[78:79], 0
	v_mov_b64_e32 v[80:81], 0
	v_mov_b64_e32 v[82:83], 0
	v_mov_b64_e32 v[84:85], 0
	v_mov_b64_e32 v[86:87], 0
	v_mov_b64_e32 v[88:89], 0
	v_mov_b64_e32 v[90:91], 0
	v_mov_b64_e32 v[92:93], 0
	v_mov_b64_e32 v[94:95], 0
	v_mov_b64_e32 v[96:97], 0
	v_mov_b64_e32 v[98:99], 0
	v_mov_b64_e32 v[100:101], 0
	v_mov_b64_e32 v[102:103], 0
	v_mov_b64_e32 v[104:105], 0
	v_mov_b64_e32 v[106:107], 0
	v_mov_b64_e32 v[108:109], 0
	v_mov_b64_e32 v[110:111], 0
	v_mov_b64_e32 v[112:113], 0
	v_mov_b64_e32 v[114:115], 0
	v_mov_b64_e32 v[116:117], 0
	v_mov_b64_e32 v[118:119], 0
	v_mov_b64_e32 v[120:121], 0
	v_mov_b64_e32 v[122:123], 0
	v_mov_b64_e32 v[124:125], 0
	v_mov_b64_e32 v[126:127], 0
	v_mov_b64_e32 v[128:129], 0
	v_mov_b64_e32 v[130:131], 0
	v_mov_b64_e32 v[132:133], 0
	v_mov_b64_e32 v[134:135], 0
	v_mov_b64_e32 v[136:137], 0
	v_mov_b64_e32 v[138:139], 0
	v_mov_b64_e32 v[140:141], 0
	v_mov_b64_e32 v[142:143], 0
	v_mov_b64_e32 v[144:145], 0
	v_mov_b64_e32 v[146:147], 0
	v_mov_b64_e32 v[148:149], 0
	v_mov_b64_e32 v[150:151], 0
	v_mov_b64_e32 v[152:153], 0
	v_mov_b64_e32 v[154:155], 0
	v_mov_b64_e32 v[156:157], 0
	v_mov_b64_e32 v[158:159], 0
	v_mov_b64_e32 v[160:161], 0
	v_mov_b64_e32 v[34:35], 0

.LBB0_2070:
	s_ashr_i32 s19, s18, 31
	s_lshl_b64 s[36:37], s[18:19], 23
	v_readlane_b32 s17, v237, 42
	s_add_u32 s19, s17, s36
	v_readlane_b32 s17, v237, 43
	s_addc_u32 s58, s17, s37
	s_ashr_i32 s17, s16, 31
	s_lshl_b64 s[36:37], s[16:17], 19
	s_add_u32 s36, s19, s36
	s_addc_u32 s37, s58, s37
	s_and_b64 s[58:59], s[54:55], exec
	s_cselect_b32 s17, s37, s57
	s_cselect_b32 s19, s36, s56
	s_add_u32 s58, s56, 0x100
	v_mov_b32_e32 v66, 0
	v_mov_b32_e32 v209, v201
	v_mov_b32_e32 v211, v201
	s_addc_u32 s59, s57, 0
	s_mov_b32 s84, -2
	s_mov_b64 s[56:57], s[24:25]
	v_mov_b64_e32 v[68:69], 0
	v_mov_b64_e32 v[70:71], 0
	v_mov_b64_e32 v[72:73], 0
	v_mov_b64_e32 v[74:75], 0
	v_mov_b64_e32 v[76:77], 0
	v_mov_b64_e32 v[78:79], 0
	v_mov_b64_e32 v[80:81], 0
	v_mov_b64_e32 v[82:83], 0
	v_mov_b64_e32 v[84:85], 0
	v_mov_b64_e32 v[86:87], 0
	v_mov_b64_e32 v[88:89], 0
	v_mov_b64_e32 v[90:91], 0
	v_mov_b64_e32 v[92:93], 0
	v_mov_b64_e32 v[94:95], 0
	v_mov_b64_e32 v[96:97], 0
	v_mov_b64_e32 v[98:99], 0
	v_mov_b64_e32 v[100:101], 0
	v_mov_b64_e32 v[102:103], 0
	v_mov_b64_e32 v[104:105], 0
	v_mov_b64_e32 v[106:107], 0
	v_mov_b64_e32 v[108:109], 0
	v_mov_b64_e32 v[110:111], 0
	v_mov_b64_e32 v[112:113], 0
	v_mov_b64_e32 v[114:115], 0
	v_mov_b64_e32 v[116:117], 0
	v_mov_b64_e32 v[118:119], 0
	v_mov_b64_e32 v[120:121], 0
	v_mov_b64_e32 v[122:123], 0
	v_mov_b64_e32 v[124:125], 0
	v_mov_b64_e32 v[126:127], 0
	v_mov_b64_e32 v[128:129], 0
	v_mov_b64_e32 v[130:131], 0
	v_mov_b64_e32 v[132:133], 0
	v_mov_b64_e32 v[134:135], 0
	v_mov_b64_e32 v[136:137], 0
	v_mov_b64_e32 v[138:139], 0
	v_mov_b64_e32 v[140:141], 0
	v_mov_b64_e32 v[142:143], 0
	v_mov_b64_e32 v[144:145], 0
	v_mov_b64_e32 v[146:147], 0
	v_mov_b64_e32 v[148:149], 0
	v_mov_b64_e32 v[150:151], 0
	v_mov_b64_e32 v[152:153], 0
	v_mov_b64_e32 v[154:155], 0
	v_mov_b64_e32 v[156:157], 0
	v_mov_b64_e32 v[158:159], 0
	v_mov_b64_e32 v[160:161], 0
	v_mov_b64_e32 v[162:163], 0
	v_mov_b64_e32 v[164:165], 0
	v_mov_b64_e32 v[166:167], 0
	v_mov_b64_e32 v[168:169], 0
	v_mov_b64_e32 v[170:171], 0
	v_mov_b64_e32 v[172:173], 0
	v_mov_b64_e32 v[174:175], 0
	v_mov_b64_e32 v[176:177], 0
	v_mov_b64_e32 v[178:179], 0
	v_mov_b64_e32 v[180:181], 0
	v_mov_b64_e32 v[182:183], 0
	v_mov_b64_e32 v[184:185], 0
	v_mov_b64_e32 v[186:187], 0
	v_mov_b64_e32 v[188:189], 0
	v_mov_b64_e32 v[190:191], 0
	v_mov_b64_e32 v[192:193], 0
	v_mov_b64_e32 v[66:67], 0
	v_lshl_or_b32 v254, s53, 7, v219
	s_mov_b32 s98, s52
	s_ashr_i32 s99, s52, 31
	s_lshl_b64 s[98:99], s[98:99], 14
	s_add_u32 s98, s40, s98
	s_addc_u32 s99, s41, s99
	v_ashrrev_i32_e32 v255, 31, v254
	v_lshl_add_u64 v[254:255], v[254:255], 2, s[98:99]
	global_load_dwordx4 v[238:241], v[254:255], off
	global_load_dwordx4 v[242:245], v[254:255], off offset:16
	v_lshl_add_u64 v[254:255], v[254:255], 0, s[42:43]
	global_load_dwordx4 v[246:249], v[254:255], off
	global_load_dwordx4 v[250:253], v[254:255], off offset:16
	s_branch .LBB0_2073

.LBB0_2150:
	s_ashr_i32 s13, s12, 31
	s_lshl_b64 s[22:23], s[12:13], 19
	s_add_u32 s24, s6, s22
	s_addc_u32 s25, s7, s23
	s_and_b64 s[22:23], s[54:55], exec
	s_cselect_b32 s13, s25, s57
	s_cselect_b32 s58, s24, s56
	s_ashr_i32 s9, s8, 31
	s_lshl_b64 s[22:23], s[8:9], 22
	s_add_u32 s9, s88, s22
	s_addc_u32 s59, s89, s23
	s_ashr_i32 s5, s4, 31
	s_lshl_b64 s[22:23], s[4:5], 19
	s_add_u32 s22, s9, s22
	s_addc_u32 s23, s59, s23
	s_and_b64 s[62:63], s[54:55], exec
	s_cselect_b32 s5, s23, s61
	s_cselect_b32 s9, s22, s60
	s_add_u32 s56, s56, 0x40080
	s_addc_u32 s57, s57, 0
	s_add_u32 s59, s60, 0x100
	v_mov_b32_e32 v34, 0
	s_addc_u32 s78, s61, 0
	s_mov_b32 s79, -2
	v_mov_b64_e32 v[36:37], 0
	v_mov_b64_e32 v[38:39], 0
	v_mov_b64_e32 v[40:41], 0
	v_mov_b64_e32 v[42:43], 0
	v_mov_b64_e32 v[44:45], 0
	v_mov_b64_e32 v[46:47], 0
	v_mov_b64_e32 v[48:49], 0
	v_mov_b64_e32 v[50:51], 0
	v_mov_b64_e32 v[52:53], 0
	v_mov_b64_e32 v[54:55], 0
	v_mov_b64_e32 v[56:57], 0
	v_mov_b64_e32 v[58:59], 0
	v_mov_b64_e32 v[60:61], 0
	v_mov_b64_e32 v[62:63], 0
	v_mov_b64_e32 v[64:65], 0
	v_mov_b64_e32 v[66:67], 0
	v_mov_b64_e32 v[68:69], 0
	v_mov_b64_e32 v[70:71], 0
	v_mov_b64_e32 v[72:73], 0
	v_mov_b64_e32 v[74:75], 0
	v_mov_b64_e32 v[76:77], 0
	v_mov_b64_e32 v[78:79], 0
	v_mov_b64_e32 v[80:81], 0
	v_mov_b64_e32 v[82:83], 0
	v_mov_b64_e32 v[84:85], 0
	v_mov_b64_e32 v[86:87], 0
	v_mov_b64_e32 v[88:89], 0
	v_mov_b64_e32 v[90:91], 0
	v_mov_b64_e32 v[92:93], 0
	v_mov_b64_e32 v[94:95], 0
	v_mov_b64_e32 v[96:97], 0
	v_mov_b64_e32 v[98:99], 0
	v_mov_b64_e32 v[100:101], 0
	v_mov_b64_e32 v[102:103], 0
	v_mov_b64_e32 v[104:105], 0
	v_mov_b64_e32 v[106:107], 0
	v_mov_b64_e32 v[108:109], 0
	v_mov_b64_e32 v[110:111], 0
	v_mov_b64_e32 v[112:113], 0
	v_mov_b64_e32 v[114:115], 0
	v_mov_b64_e32 v[116:117], 0
	v_mov_b64_e32 v[118:119], 0
	v_mov_b64_e32 v[120:121], 0
	v_mov_b64_e32 v[122:123], 0
	v_mov_b64_e32 v[124:125], 0
	v_mov_b64_e32 v[126:127], 0
	v_mov_b64_e32 v[128:129], 0
	v_mov_b64_e32 v[130:131], 0
	v_mov_b64_e32 v[132:133], 0
	v_mov_b64_e32 v[134:135], 0
	v_mov_b64_e32 v[136:137], 0
	v_mov_b64_e32 v[138:139], 0
	v_mov_b64_e32 v[140:141], 0
	v_mov_b64_e32 v[142:143], 0
	v_mov_b64_e32 v[144:145], 0
	v_mov_b64_e32 v[146:147], 0
	v_mov_b64_e32 v[148:149], 0
	v_mov_b64_e32 v[150:151], 0
	v_mov_b64_e32 v[152:153], 0
	v_mov_b64_e32 v[154:155], 0
	v_mov_b64_e32 v[156:157], 0
	v_mov_b64_e32 v[158:159], 0
	v_mov_b64_e32 v[160:161], 0
	v_mov_b64_e32 v[34:35], 0
	v_lshl_or_b32 v254, s1, 8, v183
	s_mov_b32 s98, s0
	s_ashr_i32 s99, s0, 31
	s_lshl_b64 s[98:99], s[98:99], 13
	s_add_u32 s98, s44, s98
	s_addc_u32 s99, s45, s99
	v_ashrrev_i32_e32 v255, 31, v254
	v_lshl_add_u64 v[254:255], v[254:255], 2, s[98:99]
	global_load_dwordx4 v[238:241], v[254:255], off
	global_load_dwordx4 v[242:245], v[254:255], off offset:16
	global_load_dwordx4 v[246:249], v[254:255], off offset:512
	global_load_dwordx4 v[250:253], v[254:255], off offset:528
